# attn: rowmax trimmed (cross-half combine only on rare path) and hidden under PV MFMAs, 8 exps deferred to next QK phase, younger-half prio in PV phase
# speedup vs baseline: 1.0140x; 1.0083x over previous
.Latt_pr_1:
	s_add_i32 s9, s23, s30
	v_cvt_f32_f16_e32 v58, v56
	v_cvt_f32_f16_sdwa v59, v56 dst_sel:DWORD dst_unused:UNUSED_PAD src0_sel:WORD_1
	v_add_f32_e32 v58, v59, v58
	v_add_f32_e32 v184, v199, v58
	v_lshl_add_u64 v[56:57], v[188:189], 0, s[4:5]
	s_mov_b32 m0, s9
	s_nop 0
	global_load_lds_dwordx4 v[56:57], off
	v_lshl_add_u64 v[56:57], v[188:189], 0, s[10:11]
	s_add_i32 s9, s21, s31
	s_mov_b32 m0, s9
	s_nop 0
	global_load_lds_dwordx4 v[56:57], off
	s_waitcnt lgkmcnt(14)
	v_mfma_f32_32x32x16_f16 v[0:15], v[140:143], v[176:179], v[0:15]
	v_max_f32_e32 v202, v96, v97
	v_max3_f32 v203, v98, v99, v81
	v_max3_f32 v202, v202, v80, v82
	v_max3_f32 v202, v202, v83, v100
	v_max3_f32 v203, v203, v102, v103
	v_max3_f32 v202, v202, v101, v84
	v_max3_f32 v203, v203, v86, v87
	v_max3_f32 v202, v202, v85, v104
	s_waitcnt lgkmcnt(12)
	v_mfma_f32_32x32x16_f16 v[16:31], v[140:143], v[172:175], v[16:31]
	v_max3_f32 v203, v203, v106, v107
	v_max3_f32 v202, v202, v105, v88
	v_max3_f32 v203, v203, v90, v91
	v_max3_f32 v202, v202, v89, v108
	v_max3_f32 v203, v203, v110, v111
	v_max3_f32 v202, v202, v109, v92
	v_max3_f32 v203, v203, v94, v95
	v_max3_f32 v202, v202, v93, v203
	v_add_u32_e32 v60, s21, v198
	ds_read_b128 v[56:59], v60
	ds_read_b128 v[144:147], v60 offset:512
	s_waitcnt lgkmcnt(12)
	v_mfma_f32_32x32x16_f16 v[0:15], v[132:135], v[168:171], v[0:15]
	v_cmp_lt_f32_e32 vcc, s22, v202
	s_nop 1
	s_cmp_lg_u64 vcc, 0
	s_cselect_b64 s[16:17], -1, 0
	s_nop 0
	s_cbranch_vccnz .LBB3_9
.LBB3_2:
	v_exp_f32_e32 v96, v96
	v_exp_f32_e32 v97, v97
	v_exp_f32_e32 v98, v98
	v_exp_f32_e32 v100, v100
	ds_read_b128 v[176:179], v60 offset:2048
	ds_read_b128 v[168:171], v60 offset:2560
	s_waitcnt lgkmcnt(12)
	v_mfma_f32_32x32x16_f16 v[16:31], v[132:135], v[72:75], v[16:31]
	v_exp_f32_e32 v101, v101
	v_exp_f32_e32 v102, v102
	v_exp_f32_e32 v104, v104
	v_exp_f32_e32 v105, v105
	ds_read_b128 v[172:175], v60 offset:4096
	ds_read_b128 v[160:163], v60 offset:4608
	s_waitcnt lgkmcnt(12)
	v_mfma_f32_32x32x16_f16 v[0:15], v[124:127], v[68:71], v[0:15]
	v_exp_f32_e32 v106, v106
	v_exp_f32_e32 v108, v108
	v_exp_f32_e32 v109, v109
	v_exp_f32_e32 v110, v110
	ds_read_b128 v[164:167], v60 offset:6144
	ds_read_b128 v[156:159], v60 offset:6656
	s_waitcnt lgkmcnt(12)
	v_mfma_f32_32x32x16_f16 v[16:31], v[124:127], v[64:67], v[16:31]
	v_exp_f32_e32 v80, v80
	v_exp_f32_e32 v81, v81
	v_exp_f32_e32 v82, v82
	v_exp_f32_e32 v84, v84
	s_waitcnt lgkmcnt(10)
	v_mfma_f32_32x32x16_f16 v[0:15], v[112:115], v[52:55], v[0:15]
	v_exp_f32_e32 v85, v85
	v_exp_f32_e32 v86, v86
	v_exp_f32_e32 v88, v88
	v_exp_f32_e32 v89, v89
	s_waitcnt lgkmcnt(8)
	v_mfma_f32_32x32x16_f16 v[16:31], v[112:115], v[48:51], v[16:31]
	v_exp_f32_e32 v90, v90
	v_exp_f32_e32 v92, v92
	v_exp_f32_e32 v93, v93
	v_exp_f32_e32 v94, v94
	s_waitcnt vmcnt(2) lgkmcnt(0)
	s_barrier
	s_setprio 0
	s_andn2_b64 vcc, exec, s[16:17]
	s_cbranch_vccnz .LBB3_4
	s_waitcnt lgkmcnt(0)
	v_add_u32_e32 v64, s29, v195
	ds_read_b128 v[48:51], v64 offset:49248
	ds_read_b128 v[52:55], v64 offset:49216
	ds_read_b128 v[60:63], v64 offset:49184
	ds_read_b128 v[64:67], v64 offset:49152
	s_waitcnt lgkmcnt(3)
	v_pk_mul_f32 v[12:13], v[12:13], v[48:49]
	s_waitcnt lgkmcnt(2)
	v_pk_mul_f32 v[8:9], v[8:9], v[52:53]
	s_waitcnt lgkmcnt(1)
	v_pk_mul_f32 v[4:5], v[4:5], v[60:61]
	v_pk_mul_f32 v[14:15], v[14:15], v[50:51]
	v_pk_mul_f32 v[10:11], v[10:11], v[54:55]
	v_pk_mul_f32 v[6:7], v[6:7], v[62:63]
	s_waitcnt lgkmcnt(0)
	v_pk_mul_f32 v[2:3], v[2:3], v[66:67]
	v_pk_mul_f32 v[0:1], v[0:1], v[64:65]
	v_pk_mul_f32 v[28:29], v[28:29], v[48:49]
	v_pk_mul_f32 v[24:25], v[24:25], v[52:53]
	v_pk_mul_f32 v[20:21], v[20:21], v[60:61]
	v_pk_mul_f32 v[30:31], v[30:31], v[50:51]
	v_pk_mul_f32 v[26:27], v[26:27], v[54:55]
	v_pk_mul_f32 v[22:23], v[22:23], v[62:63]
	v_pk_mul_f32 v[18:19], v[18:19], v[66:67]
	v_pk_mul_f32 v[16:17], v[16:17], v[64:65]

.Latt_pr_2:
	s_add_i32 s9, s21, s30
	v_cvt_f32_f16_e32 v90, v88
	v_cvt_f32_f16_sdwa v91, v88 dst_sel:DWORD dst_unused:UNUSED_PAD src0_sel:WORD_1
	v_add_f32_e32 v90, v91, v90
	v_add_f32_e32 v199, v184, v90
	v_lshl_add_u64 v[88:89], v[200:201], 0, s[12:13]
	s_mov_b32 m0, s9
	s_nop 0
	global_load_lds_dwordx4 v[88:89], off
	v_lshl_add_u64 v[188:189], v[188:189], 0, s[14:15]
	s_add_i32 s9, s24, s31
	s_mov_b32 m0, s9
	s_nop 0
	global_load_lds_dwordx4 v[188:189], off
	s_waitcnt lgkmcnt(14)
	v_mfma_f32_32x32x16_f16 v[0:15], v[140:143], v[152:155], v[0:15]
	v_max_f32_e32 v202, v64, v65
	v_max3_f32 v203, v66, v67, v49
	v_max3_f32 v202, v202, v48, v50
	v_max3_f32 v202, v202, v51, v68
	v_max3_f32 v203, v203, v70, v71
	v_max3_f32 v202, v202, v69, v52
	v_max3_f32 v203, v203, v54, v55
	v_max3_f32 v202, v202, v53, v72
	s_waitcnt lgkmcnt(12)
	v_mfma_f32_32x32x16_f16 v[16:31], v[140:143], v[148:151], v[16:31]
	v_max3_f32 v203, v203, v74, v75
	v_max3_f32 v202, v202, v73, v56
	v_max3_f32 v203, v203, v58, v59
	v_max3_f32 v202, v202, v57, v76
	v_max3_f32 v203, v203, v78, v79
	v_max3_f32 v202, v202, v77, v60
	v_max3_f32 v203, v203, v62, v63
	v_max3_f32 v202, v202, v61, v203
	v_add_u32_e32 v88, s24, v198
	ds_read_b128 v[172:175], v88
	ds_read_b128 v[168:171], v88 offset:512
	s_waitcnt lgkmcnt(12)
	v_mfma_f32_32x32x16_f16 v[0:15], v[132:135], v[144:147], v[0:15]
	v_cmp_lt_f32_e32 vcc, s22, v202
	s_nop 1
	s_cmp_lg_u64 vcc, 0
	s_cselect_b64 s[16:17], -1, 0
	s_nop 0
	s_cbranch_vccnz .LBB3_12
.LBB3_5:
	v_exp_f32_e32 v64, v64
	v_exp_f32_e32 v65, v65
	v_exp_f32_e32 v66, v66
	v_exp_f32_e32 v68, v68
	ds_read_b128 v[164:167], v88 offset:2048
	ds_read_b128 v[160:163], v88 offset:2560
	s_waitcnt lgkmcnt(12)
	v_mfma_f32_32x32x16_f16 v[16:31], v[132:135], v[104:107], v[16:31]
	v_exp_f32_e32 v69, v69
	v_exp_f32_e32 v70, v70
	v_exp_f32_e32 v72, v72
	v_exp_f32_e32 v73, v73
	ds_read_b128 v[156:159], v88 offset:4096
	ds_read_b128 v[152:155], v88 offset:4608
	s_waitcnt lgkmcnt(12)
	v_mfma_f32_32x32x16_f16 v[0:15], v[124:127], v[100:103], v[0:15]
	v_exp_f32_e32 v74, v74
	v_exp_f32_e32 v76, v76
	v_exp_f32_e32 v77, v77
	v_exp_f32_e32 v78, v78
	ds_read_b128 v[148:151], v88 offset:6144
	ds_read_b128 v[144:147], v88 offset:6656
	s_waitcnt lgkmcnt(12)
	v_mfma_f32_32x32x16_f16 v[16:31], v[124:127], v[96:99], v[16:31]
	v_exp_f32_e32 v48, v48
	v_exp_f32_e32 v49, v49
	v_exp_f32_e32 v50, v50
	v_exp_f32_e32 v52, v52
	s_waitcnt lgkmcnt(10)
	v_mfma_f32_32x32x16_f16 v[0:15], v[112:115], v[84:87], v[0:15]
	v_exp_f32_e32 v53, v53
	v_exp_f32_e32 v54, v54
	v_exp_f32_e32 v56, v56
	v_exp_f32_e32 v57, v57
	s_waitcnt lgkmcnt(8)
	v_mfma_f32_32x32x16_f16 v[16:31], v[112:115], v[80:83], v[16:31]
	v_exp_f32_e32 v58, v58
	v_exp_f32_e32 v60, v60
	v_exp_f32_e32 v61, v61
	v_exp_f32_e32 v62, v62
	s_waitcnt vmcnt(2) lgkmcnt(0)
	s_barrier
	s_setprio 0
	s_andn2_b64 vcc, exec, s[16:17]
	s_cbranch_vccnz .LBB3_7
	s_waitcnt lgkmcnt(0)
	v_add_u32_e32 v92, s29, v195
	ds_read_b128 v[80:83], v92 offset:49248
	ds_read_b128 v[84:87], v92 offset:49216
	ds_read_b128 v[88:91], v92 offset:49152
	ds_read_b128 v[92:95], v92 offset:49184
	s_waitcnt lgkmcnt(3)
	v_pk_mul_f32 v[14:15], v[14:15], v[82:83]
	v_pk_mul_f32 v[12:13], v[12:13], v[80:81]
	s_waitcnt lgkmcnt(2)
	v_pk_mul_f32 v[10:11], v[10:11], v[86:87]
	v_pk_mul_f32 v[8:9], v[8:9], v[84:85]
	s_waitcnt lgkmcnt(0)
	v_pk_mul_f32 v[6:7], v[6:7], v[94:95]
	v_pk_mul_f32 v[4:5], v[4:5], v[92:93]
	v_pk_mul_f32 v[2:3], v[2:3], v[90:91]
	v_pk_mul_f32 v[0:1], v[0:1], v[88:89]
	v_pk_mul_f32 v[30:31], v[30:31], v[82:83]
	v_pk_mul_f32 v[28:29], v[28:29], v[80:81]
	v_pk_mul_f32 v[26:27], v[26:27], v[86:87]
	v_pk_mul_f32 v[24:25], v[24:25], v[84:85]
	v_pk_mul_f32 v[22:23], v[22:23], v[94:95]
	v_pk_mul_f32 v[20:21], v[20:21], v[92:93]
	v_pk_mul_f32 v[18:19], v[18:19], v[90:91]
	v_pk_mul_f32 v[16:17], v[16:17], v[88:89]

.LBB3_9:
	v_mov_b32_e32 v203, v202
	s_nop 1
	v_permlane32_swap_b32_e32 v202, v203
	v_max_f32_e32 v202, v202, v203
	v_max_f32_e32 v32, v202, v202
	v_max_f32_e32 v202, 0, v32
	v_exp_f32_e64 v203, -v202
	v_add_f32_e32 v197, v197, v202
	v_xor_b32_e32 v32, 0x80000000, v197
	v_mov_b32_e32 v33, v32
	v_mov_b32_e32 v34, v32
	v_mov_b32_e32 v35, v32
	v_mov_b32_e32 v36, v32
	v_mov_b32_e32 v37, v32
	v_mov_b32_e32 v38, v32
	v_mov_b32_e32 v39, v32
	v_mov_b32_e32 v40, v32
	v_mov_b32_e32 v41, v32
	v_mov_b32_e32 v42, v32
	v_mov_b32_e32 v43, v32
	v_mov_b32_e32 v44, v32
	v_mov_b32_e32 v45, v32
	v_mov_b32_e32 v46, v32
	v_mov_b32_e32 v47, v32
	s_and_saveexec_b64 s[18:19], s[0:1]
	ds_write_b32 v196, v203 offset:49152
	s_or_b64 exec, exec, s[18:19]
	v_sub_f32_e32 v111, v111, v202
	v_sub_f32_e32 v110, v110, v202
	v_sub_f32_e32 v109, v109, v202
	v_sub_f32_e32 v108, v108, v202
	v_sub_f32_e32 v107, v107, v202
	v_sub_f32_e32 v106, v106, v202
	v_sub_f32_e32 v105, v105, v202
	v_sub_f32_e32 v104, v104, v202
	v_sub_f32_e32 v103, v103, v202
	v_sub_f32_e32 v102, v102, v202
	v_sub_f32_e32 v101, v101, v202
	v_sub_f32_e32 v100, v100, v202
	v_sub_f32_e32 v99, v99, v202
	v_sub_f32_e32 v98, v98, v202
	v_sub_f32_e32 v97, v97, v202
	v_sub_f32_e32 v96, v96, v202
	v_sub_f32_e32 v95, v95, v202
	v_sub_f32_e32 v94, v94, v202
	v_sub_f32_e32 v93, v93, v202
	v_sub_f32_e32 v92, v92, v202
	v_sub_f32_e32 v91, v91, v202
	v_sub_f32_e32 v90, v90, v202
	v_sub_f32_e32 v89, v89, v202
	v_sub_f32_e32 v88, v88, v202
	v_sub_f32_e32 v87, v87, v202
	v_sub_f32_e32 v86, v86, v202
	v_sub_f32_e32 v85, v85, v202
	v_sub_f32_e32 v84, v84, v202
	v_sub_f32_e32 v83, v83, v202
	v_sub_f32_e32 v82, v82, v202
	v_sub_f32_e32 v81, v81, v202
	v_sub_f32_e32 v80, v80, v202
	v_mul_f32_e32 v184, v184, v203
	s_branch .LBB3_2
.LBB3_12:
	v_mov_b32_e32 v203, v202
	s_nop 1
	v_permlane32_swap_b32_e32 v202, v203
	v_max_f32_e32 v202, v202, v203
	v_max_f32_e32 v32, v202, v202
	v_max_f32_e32 v202, 0, v32
	v_exp_f32_e64 v203, -v202
	v_add_f32_e32 v197, v197, v202
	v_xor_b32_e32 v32, 0x80000000, v197
	v_mov_b32_e32 v33, v32
	v_mov_b32_e32 v34, v32
	v_mov_b32_e32 v35, v32
	v_mov_b32_e32 v36, v32
	v_mov_b32_e32 v37, v32
	v_mov_b32_e32 v38, v32
	v_mov_b32_e32 v39, v32
	v_mov_b32_e32 v40, v32
	v_mov_b32_e32 v41, v32
	v_mov_b32_e32 v42, v32
	v_mov_b32_e32 v43, v32
	v_mov_b32_e32 v44, v32
	v_mov_b32_e32 v45, v32
	v_mov_b32_e32 v46, v32
	v_mov_b32_e32 v47, v32
	s_and_saveexec_b64 s[18:19], s[0:1]
	ds_write_b32 v196, v203 offset:49152
	s_or_b64 exec, exec, s[18:19]
	v_sub_f32_e32 v79, v79, v202
	v_sub_f32_e32 v78, v78, v202
	v_sub_f32_e32 v77, v77, v202
	v_sub_f32_e32 v76, v76, v202
	v_sub_f32_e32 v75, v75, v202
	v_sub_f32_e32 v74, v74, v202
	v_sub_f32_e32 v73, v73, v202
	v_sub_f32_e32 v72, v72, v202
	v_sub_f32_e32 v71, v71, v202
	v_sub_f32_e32 v70, v70, v202
	v_sub_f32_e32 v69, v69, v202
	v_sub_f32_e32 v68, v68, v202
	v_sub_f32_e32 v67, v67, v202
	v_sub_f32_e32 v66, v66, v202
	v_sub_f32_e32 v65, v65, v202
	v_sub_f32_e32 v64, v64, v202
	v_sub_f32_e32 v63, v63, v202
	v_sub_f32_e32 v62, v62, v202
	v_sub_f32_e32 v61, v61, v202
	v_sub_f32_e32 v60, v60, v202
	v_sub_f32_e32 v59, v59, v202
	v_sub_f32_e32 v58, v58, v202
	v_sub_f32_e32 v57, v57, v202
	v_sub_f32_e32 v56, v56, v202
	v_sub_f32_e32 v55, v55, v202
	v_sub_f32_e32 v54, v54, v202
	v_sub_f32_e32 v53, v53, v202
	v_sub_f32_e32 v52, v52, v202
	v_sub_f32_e32 v51, v51, v202
	v_sub_f32_e32 v50, v50, v202
	v_sub_f32_e32 v49, v49, v202
	v_sub_f32_e32 v48, v48, v202
	v_mul_f32_e32 v199, v199, v203
	s_branch .LBB3_5
